# baseline (speedup 1.0000x reference)
_Z14combine_kernelPKDF16_PKfPf:
	s_load_dwordx4 s[4:7], s[0:1], 0x0
	s_load_dwordx2 s[10:11], s[0:1], 0x10
	s_lshl_b32 s3, s2, 5
	s_and_b32 s3, s3, 0x60
	s_lshr_b32 s8, s2, 5
	s_add_i32 s8, s8, s3
	s_lshl_b32 s9, s8, 5
	s_getpc_b64 s[12:13]
	s_add_u32 s12, s12, g_tab@rel32@lo+4
	s_addc_u32 s13, s13, g_tab@rel32@hi+12
	s_add_u32 s12, s12, s9
	s_addc_u32 s13, s13, 0
	s_load_dwordx8 s[16:23], s[12:13], 0x1a60
	s_lshl_b32 s2, s2, 2
	s_and_b32 s2, s2, 0x70
	v_lshrrev_b32_e32 v1, 4, v0
	v_or_b32_e32 v38, s2, v1
	v_lshlrev_b32_e32 v2, 2, v0
	v_and_b32_e32 v39, 60, v2
	v_lshlrev_b32_e32 v32, 3, v38
	v_lshlrev_b32_e32 v33, 7, v38
	v_lshl_add_u32 v33, v39, 1, v33
	v_lshlrev_b32_e32 v45, 8, v38
	v_lshl_add_u32 v45, v39, 2, v45
	s_add_i32 s0, s8, 3
	s_lshl_b32 s0, s0, 15
	s_mov_b32 s14, 0x7f800000
	s_mov_b32 s15, 0xf149f2ca
	s_waitcnt lgkmcnt(0)
	s_cmp_lt_i32 s17, 0
	s_cbranch_scc1 .Lcomb_end
	s_add_u32 s10, s10, s0
	s_addc_u32 s11, s11, 0
	s_lshl_b32 s24, s16, 10
	s_lshl_b32 s26, s16, 14
	s_add_u32 s24, s6, s24
	s_addc_u32 s25, s7, 0
	s_add_u32 s26, s4, s26
	s_addc_u32 s27, s5, 0
	global_load_dwordx2 v[0:1], v32, s[24:25] nt
	global_load_dwordx2 v[16:17], v33, s[26:27] nt
	s_lshl_b32 s28, s17, 10
	s_lshl_b32 s30, s17, 14
	s_add_u32 s28, s6, s28
	s_addc_u32 s29, s7, 0
	s_add_u32 s30, s4, s30
	s_addc_u32 s31, s5, 0
	global_load_dwordx2 v[2:3], v32, s[28:29] nt
	global_load_dwordx2 v[18:19], v33, s[30:31] nt
	s_cmp_lt_i32 s18, 0
	s_cselect_b32 s58, s15, s14
	s_cselect_b32 s1, s16, s18
	s_lshl_b32 s32, s1, 10
	s_lshl_b32 s34, s1, 14
	s_add_u32 s32, s6, s32
	s_addc_u32 s33, s7, 0
	s_add_u32 s34, s4, s34
	s_addc_u32 s35, s5, 0
	global_load_dwordx2 v[4:5], v32, s[32:33] nt
	global_load_dwordx2 v[20:21], v33, s[34:35] nt
	s_cmp_lt_i32 s19, 0
	s_cselect_b32 s59, s15, s14
	s_cselect_b32 s1, s16, s19
	s_lshl_b32 s36, s1, 10
	s_lshl_b32 s38, s1, 14
	s_add_u32 s36, s6, s36
	s_addc_u32 s37, s7, 0
	s_add_u32 s38, s4, s38
	s_addc_u32 s39, s5, 0
	global_load_dwordx2 v[6:7], v32, s[36:37] nt
	global_load_dwordx2 v[22:23], v33, s[38:39] nt
	s_cmp_lt_i32 s20, 0
	s_cselect_b32 s60, s15, s14
	s_cselect_b32 s1, s16, s20
	s_lshl_b32 s40, s1, 10
	s_lshl_b32 s42, s1, 14
	s_add_u32 s40, s6, s40
	s_addc_u32 s41, s7, 0
	s_add_u32 s42, s4, s42
	s_addc_u32 s43, s5, 0
	global_load_dwordx2 v[8:9], v32, s[40:41] nt
	global_load_dwordx2 v[24:25], v33, s[42:43] nt
	s_cmp_lt_i32 s21, 0
	s_cselect_b32 s61, s15, s14
	s_cselect_b32 s1, s16, s21
	s_lshl_b32 s44, s1, 10
	s_lshl_b32 s46, s1, 14
	s_add_u32 s44, s6, s44
	s_addc_u32 s45, s7, 0
	s_add_u32 s46, s4, s46
	s_addc_u32 s47, s5, 0
	global_load_dwordx2 v[10:11], v32, s[44:45] nt
	global_load_dwordx2 v[26:27], v33, s[46:47] nt
	s_cmp_lt_i32 s22, 0
	s_cselect_b32 s62, s15, s14
	s_cselect_b32 s1, s16, s22
	s_lshl_b32 s48, s1, 10
	s_lshl_b32 s50, s1, 14
	s_add_u32 s48, s6, s48
	s_addc_u32 s49, s7, 0
	s_add_u32 s50, s4, s50
	s_addc_u32 s51, s5, 0
	global_load_dwordx2 v[12:13], v32, s[48:49] nt
	global_load_dwordx2 v[28:29], v33, s[50:51] nt
	s_cmp_lt_i32 s23, 0
	s_cselect_b32 s63, s15, s14
	s_cselect_b32 s1, s16, s23
	s_lshl_b32 s52, s1, 10
	s_lshl_b32 s54, s1, 14
	s_add_u32 s52, s6, s52
	s_addc_u32 s53, s7, 0
	s_add_u32 s54, s4, s54
	s_addc_u32 s55, s5, 0
	global_load_dwordx2 v[14:15], v32, s[52:53] nt
	global_load_dwordx2 v[30:31], v33, s[54:55] nt
	s_waitcnt vmcnt(0)
	v_min_f32_e32 v4, s58, v4
	v_min_f32_e32 v6, s59, v6
	v_min_f32_e32 v8, s60, v8
	v_min_f32_e32 v10, s61, v10
	v_min_f32_e32 v12, s62, v12
	v_min_f32_e32 v14, s63, v14
	v_max3_f32 v34, v0, v2, v4
	v_max3_f32 v34, v34, v6, v8
	v_max3_f32 v34, v34, v10, v12
	v_max_f32_e32 v34, v34, v14
	v_sub_f32_e32 v0, v0, v34
	v_sub_f32_e32 v2, v2, v34
	v_sub_f32_e32 v4, v4, v34
	v_sub_f32_e32 v6, v6, v34
	v_sub_f32_e32 v8, v8, v34
	v_sub_f32_e32 v10, v10, v34
	v_sub_f32_e32 v12, v12, v34
	v_sub_f32_e32 v14, v14, v34
	v_exp_f32_e32 v0, v0
	v_exp_f32_e32 v2, v2
	v_exp_f32_e32 v4, v4
	v_exp_f32_e32 v6, v6
	v_exp_f32_e32 v8, v8
	v_exp_f32_e32 v10, v10
	v_exp_f32_e32 v12, v12
	v_exp_f32_e32 v14, v14
	s_nop 0
	v_mul_f32_e32 v0, v0, v1
	v_mul_f32_e32 v2, v2, v3
	v_mul_f32_e32 v4, v4, v5
	v_mul_f32_e32 v6, v6, v7
	v_mul_f32_e32 v8, v8, v9
	v_mul_f32_e32 v10, v10, v11
	v_mul_f32_e32 v12, v12, v13
	v_mul_f32_e32 v14, v14, v15
	v_cvt_f32_f16_e32 v40, v16
	v_cvt_f32_f16_sdwa v41, v16 dst_sel:DWORD dst_unused:UNUSED_PAD src0_sel:WORD_1
	v_cvt_f32_f16_e32 v42, v17
	v_cvt_f32_f16_sdwa v43, v17 dst_sel:DWORD dst_unused:UNUSED_PAD src0_sel:WORD_1
	v_mul_f32_e32 v34, v40, v0
	v_mul_f32_e32 v35, v41, v0
	v_mul_f32_e32 v36, v42, v0
	v_mul_f32_e32 v37, v43, v0
	v_mov_b32_e32 v44, v0
	v_cvt_f32_f16_e32 v40, v18
	v_cvt_f32_f16_sdwa v41, v18 dst_sel:DWORD dst_unused:UNUSED_PAD src0_sel:WORD_1
	v_cvt_f32_f16_e32 v42, v19
	v_cvt_f32_f16_sdwa v43, v19 dst_sel:DWORD dst_unused:UNUSED_PAD src0_sel:WORD_1
	v_fmac_f32_e32 v34, v40, v2
	v_fmac_f32_e32 v35, v41, v2
	v_fmac_f32_e32 v36, v42, v2
	v_fmac_f32_e32 v37, v43, v2
	v_add_f32_e32 v44, v44, v2
	s_cmp_lt_i32 s18, 0
	s_cbranch_scc1 .Lcomb_fin
	v_cvt_f32_f16_e32 v40, v20
	v_cvt_f32_f16_sdwa v41, v20 dst_sel:DWORD dst_unused:UNUSED_PAD src0_sel:WORD_1
	v_cvt_f32_f16_e32 v42, v21
	v_cvt_f32_f16_sdwa v43, v21 dst_sel:DWORD dst_unused:UNUSED_PAD src0_sel:WORD_1
	v_fmac_f32_e32 v34, v40, v4
	v_fmac_f32_e32 v35, v41, v4
	v_fmac_f32_e32 v36, v42, v4
	v_fmac_f32_e32 v37, v43, v4
	v_add_f32_e32 v44, v44, v4
	s_cmp_lt_i32 s19, 0
	s_cbranch_scc1 .Lcomb_fin
	v_cvt_f32_f16_e32 v40, v22
	v_cvt_f32_f16_sdwa v41, v22 dst_sel:DWORD dst_unused:UNUSED_PAD src0_sel:WORD_1
	v_cvt_f32_f16_e32 v42, v23
	v_cvt_f32_f16_sdwa v43, v23 dst_sel:DWORD dst_unused:UNUSED_PAD src0_sel:WORD_1
	v_fmac_f32_e32 v34, v40, v6
	v_fmac_f32_e32 v35, v41, v6
	v_fmac_f32_e32 v36, v42, v6
	v_fmac_f32_e32 v37, v43, v6
	v_add_f32_e32 v44, v44, v6
	s_cmp_lt_i32 s20, 0
	s_cbranch_scc1 .Lcomb_fin
	v_cvt_f32_f16_e32 v40, v24
	v_cvt_f32_f16_sdwa v41, v24 dst_sel:DWORD dst_unused:UNUSED_PAD src0_sel:WORD_1
	v_cvt_f32_f16_e32 v42, v25
	v_cvt_f32_f16_sdwa v43, v25 dst_sel:DWORD dst_unused:UNUSED_PAD src0_sel:WORD_1
	v_fmac_f32_e32 v34, v40, v8
	v_fmac_f32_e32 v35, v41, v8
	v_fmac_f32_e32 v36, v42, v8
	v_fmac_f32_e32 v37, v43, v8
	v_add_f32_e32 v44, v44, v8
	s_cmp_lt_i32 s21, 0
	s_cbranch_scc1 .Lcomb_fin
	v_cvt_f32_f16_e32 v40, v26
	v_cvt_f32_f16_sdwa v41, v26 dst_sel:DWORD dst_unused:UNUSED_PAD src0_sel:WORD_1
	v_cvt_f32_f16_e32 v42, v27
	v_cvt_f32_f16_sdwa v43, v27 dst_sel:DWORD dst_unused:UNUSED_PAD src0_sel:WORD_1
	v_fmac_f32_e32 v34, v40, v10
	v_fmac_f32_e32 v35, v41, v10
	v_fmac_f32_e32 v36, v42, v10
	v_fmac_f32_e32 v37, v43, v10
	v_add_f32_e32 v44, v44, v10
	s_cmp_lt_i32 s22, 0
	s_cbranch_scc1 .Lcomb_fin
	v_cvt_f32_f16_e32 v40, v28
	v_cvt_f32_f16_sdwa v41, v28 dst_sel:DWORD dst_unused:UNUSED_PAD src0_sel:WORD_1
	v_cvt_f32_f16_e32 v42, v29
	v_cvt_f32_f16_sdwa v43, v29 dst_sel:DWORD dst_unused:UNUSED_PAD src0_sel:WORD_1
	v_fmac_f32_e32 v34, v40, v12
	v_fmac_f32_e32 v35, v41, v12
	v_fmac_f32_e32 v36, v42, v12
	v_fmac_f32_e32 v37, v43, v12
	v_add_f32_e32 v44, v44, v12
	s_cmp_lt_i32 s23, 0
	s_cbranch_scc1 .Lcomb_fin
	v_cvt_f32_f16_e32 v40, v30
	v_cvt_f32_f16_sdwa v41, v30 dst_sel:DWORD dst_unused:UNUSED_PAD src0_sel:WORD_1
	v_cvt_f32_f16_e32 v42, v31
	v_cvt_f32_f16_sdwa v43, v31 dst_sel:DWORD dst_unused:UNUSED_PAD src0_sel:WORD_1
	v_fmac_f32_e32 v34, v40, v14
	v_fmac_f32_e32 v35, v41, v14
	v_fmac_f32_e32 v36, v42, v14
	v_fmac_f32_e32 v37, v43, v14
	v_add_f32_e32 v44, v44, v14
.Lcomb_fin:
	v_div_scale_f32 v14, s[0:1], v44, v44, 1.0
	v_div_scale_f32 v2, vcc, 1.0, v44, 1.0
	v_rcp_f32_e32 v15, v14
	s_nop 0
	v_fma_f32 v3, -v14, v15, 1.0
	v_fmac_f32_e32 v15, v3, v15
	v_mul_f32_e32 v3, v2, v15
	v_fma_f32 v6, -v14, v3, v2
	v_fmac_f32_e32 v3, v6, v15
	v_fma_f32 v2, -v14, v3, v2
	v_div_fmas_f32 v2, v2, v15, v3
	v_div_fixup_f32 v6, v2, v44, 1.0
	v_mul_f32_e32 v34, v34, v6
	v_mul_f32_e32 v35, v35, v6
	v_mul_f32_e32 v36, v36, v6
	v_mul_f32_e32 v37, v37, v6
	global_store_dwordx4 v45, v[34:37], s[10:11] sc1
